# P5/P6: leading half's align barrier moved ~60 instructions into the tile epilogue (starts its epilogue under the trailing half's last MFMA block); m1
# baseline (speedup 1.0000x reference)
; #define LAS __attribute__((address_space(3)))
; __device__ __forceinline__ unsigned cvt_pk_bf16(float lo, float hi) { return cvt2bf(lo, hi); }
;     __device__ __forceinline__ void operator()(const f32x4 (&acc)[2][2][4][2], const Unit& u, int wr, int wc, int fr, int fq, float b1, LAS float* bx) const {
;         const int row0 = u.pm * BM + wr * 64 + fr, col0 = u.pn * HALF + wc * 32 + 8 * fq;
;         bx[threadIdx.x & 63] = b1;
;         const f32x4 g0 = *(const LAS f32x4*)(bx + 8 * fq), g1 = *(const LAS f32x4*)(bx + 8 * fq + 4), u0 = *(const LAS f32x4*)(bx + 32 + 8 * fq), u1 = *(const LAS f32x4*)(bx + 36 + 8 * fq);
; #pragma unroll
;         for (int ai = 0; ai < 2; ++ai)
; #pragma unroll
;             for (int m = 0; m < 4; ++m) {
;                 bf16* rowp = act + (size_t)(row0 + ai * HALF + m * 16) * DM + col0;
;                 float o[8];
; #pragma unroll
;                 for (int n = 0; n < 2; ++n)
; #pragma unroll
;                     for (int j = 0; j < 4; j += 2) {
;                         const f32x4 gb = n ? g1 : g0, ub = n ? u1 : u0;
;                         const f32x2_t hg = f32x2_t{acc[ai][0][m][n][j], acc[ai][0][m][n][j + 1]} + f32x2_t{gb[j], gb[j + 1]};
;                         const f32x2_t hu = f32x2_t{acc[ai][1][m][n][j], acc[ai][1][m][n][j + 1]} + f32x2_t{ub[j], ub[j + 1]};
;                         const f32x2_t gt = {fminf(hg[0], 7.0f), fminf(hg[1], 7.0f)}, up = {fminf(fmaxf(hu[0], -7.0f), 7.0f), fminf(fmaxf(hu[1], -7.0f), 7.0f)};
;                         const f32x2_t t = gt * (-1.702f * 1.4426950408889634f);
;                         const f32x2_t dn = f32x2_t{__builtin_amdgcn_exp2f(t[0]), __builtin_amdgcn_exp2f(t[1])} + 1.0f;
;                         const f32x2_t sg = {__builtin_amdgcn_rcpf(dn[0]), __builtin_amdgcn_rcpf(dn[1])};
;                         const f32x2_t r2 = (up * gt + gt) * sg;
;                         o[n * 4 + j] = r2[0]; o[n * 4 + j + 1] = r2[1]; }
;                 v4u w; w.x = cvt_pk_bf16(o[0], o[1]); w.y = cvt_pk_bf16(o[2], o[3]); w.z = cvt_pk_bf16(o[4], o[5]); w.w = cvt_pk_bf16(o[6], o[7]);
;                 *(v4u*)rowp = w; }
.LBB0_1248:
	s_waitcnt vmcnt(8)
	ds_write_b32 v168, v130
	ds_read_b128 v[142:145], v169
	ds_read_b128 v[134:137], v169 offset:16
	ds_read_b128 v[138:141], v169 offset:128
	ds_read_b128 v[130:133], v169 offset:144
	v_lshl_add_u32 v154, s84, 8, v1
	s_waitcnt lgkmcnt(3)
	v_pk_add_f32 v[128:129], v[128:129], v[144:145]
	v_pk_add_f32 v[126:127], v[126:127], v[142:143]
	v_min_f32_e32 v128, 0x40e00000, v128
	v_min_f32_e32 v129, 0x40e00000, v129
	v_pk_mul_f32 v[178:179], v[128:129], s[26:27] op_sel_hi:[1,0]
	s_waitcnt lgkmcnt(1)
	v_pk_add_f32 v[118:119], v[118:119], v[138:139]
	v_exp_f32_e32 v178, v178
	v_exp_f32_e32 v179, v179
	v_min_f32_e32 v126, 0x40e00000, v126
	v_min_f32_e32 v127, 0x40e00000, v127
	v_med3_f32 v118, v118, s63, v167
	v_med3_f32 v119, v119, s63, v167
	v_pk_mul_f32 v[176:177], v[126:127], s[26:27] op_sel_hi:[1,0]
	v_pk_fma_f32 v[118:119], v[126:127], v[118:119], v[126:127]
	v_pk_add_f32 v[126:127], v[178:179], 1.0 op_sel_hi:[1,0]
	v_pk_add_f32 v[120:121], v[120:121], v[140:141]
	v_rcp_f32_e32 v126, v126
	v_rcp_f32_e32 v127, v127
	v_med3_f32 v120, v120, s63, v167
	v_med3_f32 v121, v121, s63, v167
	v_pk_add_f32 v[122:123], v[122:123], v[134:135]
	v_pk_fma_f32 v[120:121], v[128:129], v[120:121], v[128:129]
	v_min_f32_e32 v122, 0x40e00000, v122
	v_min_f32_e32 v123, 0x40e00000, v123
	v_pk_mul_f32 v[120:121], v[120:121], v[126:127]
	v_pk_mul_f32 v[126:127], v[122:123], s[26:27] op_sel_hi:[1,0]
	v_exp_f32_e32 v176, v176
	v_exp_f32_e32 v126, v126
	v_exp_f32_e32 v127, v127
	v_exp_f32_e32 v177, v177
	v_pk_add_f32 v[124:125], v[124:125], v[136:137]
	s_waitcnt lgkmcnt(0)
	v_pk_add_f32 v[110:111], v[110:111], v[130:131]
	v_min_f32_e32 v124, 0x40e00000, v124
	v_min_f32_e32 v125, 0x40e00000, v125
	v_pk_add_f32 v[126:127], v[126:127], 1.0 op_sel_hi:[1,0]
	v_pk_mul_f32 v[128:129], v[124:125], s[26:27] op_sel_hi:[1,0]
	v_pk_add_f32 v[176:177], v[176:177], 1.0 op_sel_hi:[1,0]
	v_rcp_f32_e32 v126, v126
	v_rcp_f32_e32 v127, v127
	v_exp_f32_e32 v128, v128
	v_exp_f32_e32 v129, v129
	v_rcp_f32_e32 v176, v176
	v_rcp_f32_e32 v177, v177
	v_med3_f32 v110, v110, s63, v167
	v_med3_f32 v111, v111, s63, v167
	v_pk_fma_f32 v[110:111], v[122:123], v[110:111], v[122:123]
	v_pk_add_f32 v[104:105], v[104:105], v[144:145]
	v_pk_mul_f32 v[122:123], v[110:111], v[126:127]
	v_pk_add_f32 v[110:111], v[128:129], 1.0 op_sel_hi:[1,0]
	v_pk_mul_f32 v[118:119], v[118:119], v[176:177]
	v_rcp_f32_e32 v110, v110
	v_rcp_f32_e32 v111, v111
	s_cmpk_gt_u32 s47, 0xff
	s_cbranch_scc1 .Lp5_al
	s_barrier
.Lp5_al:
	v_min_f32_e32 v104, 0x40e00000, v104
	v_min_f32_e32 v105, 0x40e00000, v105
	v_pk_add_f32 v[112:113], v[112:113], v[132:133]
	v_cvt_pk_bf16_f32 v118, v118, v119
	v_cvt_pk_bf16_f32 v119, v120, v121
	v_cvt_pk_bf16_f32 v120, v122, v123
	v_pk_mul_f32 v[122:123], v[104:105], s[26:27] op_sel_hi:[1,0]
	v_lshl_or_b32 v172, s36, 7, v170
	v_ashrrev_i32_e32 v155, 31, v154
	v_med3_f32 v112, v112, s63, v167
	v_med3_f32 v113, v113, s63, v167
	v_exp_f32_e32 v122, v122
	v_exp_f32_e32 v123, v123
	v_ashrrev_i32_e32 v173, 31, v172
	v_lshlrev_b64 v[174:175], 12, v[154:155]
	v_pk_fma_f32 v[112:113], v[124:125], v[112:113], v[124:125]
	v_lshl_add_u64 v[174:175], s[12:13], 0, v[174:175]
	v_pk_mul_f32 v[124:125], v[112:113], v[110:111]
	v_lshlrev_b64 v[112:113], 1, v[172:173]
	v_pk_add_f32 v[102:103], v[102:103], v[142:143]
	v_pk_add_f32 v[86:87], v[86:87], v[138:139]
	v_lshl_add_u64 v[110:111], v[174:175], 0, v[112:113]
	v_cvt_pk_bf16_f32 v121, v124, v125
	v_min_f32_e32 v102, 0x40e00000, v102
	v_min_f32_e32 v103, 0x40e00000, v103
	v_med3_f32 v86, v86, s63, v167
	v_med3_f32 v87, v87, s63, v167
	global_store_dwordx4 v[110:111], v[118:121], off
	v_pk_fma_f32 v[86:87], v[102:103], v[86:87], v[102:103]
	v_pk_add_f32 v[88:89], v[88:89], v[140:141]
	v_pk_mul_f32 v[120:121], v[102:103], s[26:27] op_sel_hi:[1,0]
	v_pk_add_f32 v[102:103], v[122:123], 1.0 op_sel_hi:[1,0]
	v_med3_f32 v88, v88, s63, v167
	v_rcp_f32_e32 v102, v102
	v_rcp_f32_e32 v103, v103
	v_med3_f32 v89, v89, s63, v167
	v_pk_add_f32 v[90:91], v[90:91], v[134:135]
	v_pk_fma_f32 v[88:89], v[104:105], v[88:89], v[104:105]
	v_min_f32_e32 v90, 0x40e00000, v90
	v_min_f32_e32 v91, 0x40e00000, v91
	v_pk_mul_f32 v[88:89], v[88:89], v[102:103]
	v_pk_mul_f32 v[102:103], v[90:91], s[26:27] op_sel_hi:[1,0]
	v_pk_add_f32 v[92:93], v[92:93], v[136:137]
	v_exp_f32_e32 v102, v102
	v_exp_f32_e32 v103, v103
	v_min_f32_e32 v92, 0x40e00000, v92
	v_min_f32_e32 v93, 0x40e00000, v93
	v_exp_f32_e32 v120, v120
	v_exp_f32_e32 v121, v121
	v_pk_add_f32 v[102:103], v[102:103], 1.0 op_sel_hi:[1,0]
	v_pk_mul_f32 v[104:105], v[92:93], s[26:27] op_sel_hi:[1,0]
	v_rcp_f32_e32 v102, v102
	v_rcp_f32_e32 v103, v103
	v_exp_f32_e32 v104, v104
	v_exp_f32_e32 v105, v105
	v_pk_add_f32 v[74:75], v[74:75], v[130:131]
	v_pk_add_f32 v[120:121], v[120:121], 1.0 op_sel_hi:[1,0]
	v_med3_f32 v74, v74, s63, v167
	v_med3_f32 v75, v75, s63, v167
	v_pk_fma_f32 v[74:75], v[90:91], v[74:75], v[90:91]
	v_rcp_f32_e32 v120, v120
	v_rcp_f32_e32 v121, v121
	v_pk_mul_f32 v[90:91], v[74:75], v[102:103]
	v_pk_add_f32 v[74:75], v[104:105], 1.0 op_sel_hi:[1,0]
	v_pk_add_f32 v[76:77], v[76:77], v[132:133]
	v_rcp_f32_e32 v74, v74
	v_rcp_f32_e32 v75, v75
	v_med3_f32 v76, v76, s63, v167
	v_med3_f32 v77, v77, s63, v167
	v_pk_add_f32 v[72:73], v[72:73], v[144:145]
	v_pk_mul_f32 v[86:87], v[86:87], v[120:121]
	v_pk_fma_f32 v[76:77], v[92:93], v[76:77], v[92:93]
	v_min_f32_e32 v72, 0x40e00000, v72
	v_min_f32_e32 v73, 0x40e00000, v73
	v_or_b32_e32 v118, 16, v154
	v_pk_mul_f32 v[92:93], v[76:77], v[74:75]
	v_cvt_pk_bf16_f32 v74, v86, v87
	v_pk_mul_f32 v[86:87], v[72:73], s[26:27] op_sel_hi:[1,0]
	v_ashrrev_i32_e32 v119, 31, v118
; __device__ __forceinline__ unsigned cvt_pk_bf16(float lo, float hi) { return cvt2bf(lo, hi); }
;     __device__ __forceinline__ void operator()(const f32x4 (&acc)[2][2][4][2], const Unit& u, int wr, int wc, int fr, int fq, float b1, LAS float* bx) const {
;     ...
; #pragma unroll
;         for (int ai = 0; ai < 2; ++ai)
; #pragma unroll
;             for (int m = 0; m < 4; ++m) {
;                 bf16* rowp = act + (size_t)(row0 + ai * HALF + m * 16) * DM + col0;
;                 float o[8];
; #pragma unroll
;                 for (int n = 0; n < 2; ++n)
; #pragma unroll
;                     for (int j = 0; j < 4; j += 2) {
;                         const f32x4 gb = n ? g1 : g0, ub = n ? u1 : u0;
;                         const f32x2_t hg = f32x2_t{acc[ai][0][m][n][j], acc[ai][0][m][n][j + 1]} + f32x2_t{gb[j], gb[j + 1]};
;                         const f32x2_t hu = f32x2_t{acc[ai][1][m][n][j], acc[ai][1][m][n][j + 1]} + f32x2_t{ub[j], ub[j + 1]};
;                         const f32x2_t gt = {fminf(hg[0], 7.0f), fminf(hg[1], 7.0f)}, up = {fminf(fmaxf(hu[0], -7.0f), 7.0f), fminf(fmaxf(hu[1], -7.0f), 7.0f)};
;                         const f32x2_t t = gt * (-1.702f * 1.4426950408889634f);
;                         const f32x2_t dn = f32x2_t{__builtin_amdgcn_exp2f(t[0]), __builtin_amdgcn_exp2f(t[1])} + 1.0f;
;                         const f32x2_t sg = {__builtin_amdgcn_rcpf(dn[0]), __builtin_amdgcn_rcpf(dn[1])};
;                         const f32x2_t r2 = (up * gt + gt) * sg;
;                         o[n * 4 + j] = r2[0]; o[n * 4 + j + 1] = r2[1]; }
;                 v4u w; w.x = cvt_pk_bf16(o[0], o[1]); w.y = cvt_pk_bf16(o[2], o[3]); w.z = cvt_pk_bf16(o[4], o[5]); w.w = cvt_pk_bf16(o[6], o[7]);
;                 *(v4u*)rowp = w; }
	v_exp_f32_e32 v86, v86
	v_exp_f32_e32 v87, v87
	v_lshlrev_b64 v[118:119], 12, v[118:119]
	v_lshl_add_u64 v[118:119], s[12:13], 0, v[118:119]
	v_pk_add_f32 v[70:71], v[70:71], v[142:143]
	v_pk_add_f32 v[54:55], v[54:55], v[138:139]
	v_lshl_add_u64 v[102:103], v[118:119], 0, v[112:113]
	v_cvt_pk_bf16_f32 v75, v88, v89
	v_cvt_pk_bf16_f32 v76, v90, v91
	v_cvt_pk_bf16_f32 v77, v92, v93
	v_min_f32_e32 v70, 0x40e00000, v70
	v_min_f32_e32 v71, 0x40e00000, v71
	v_med3_f32 v54, v54, s63, v167
	v_med3_f32 v55, v55, s63, v167
	global_store_dwordx4 v[102:103], v[74:77], off
	v_pk_fma_f32 v[54:55], v[70:71], v[54:55], v[70:71]
	v_pk_add_f32 v[56:57], v[56:57], v[140:141]
	v_pk_mul_f32 v[76:77], v[70:71], s[26:27] op_sel_hi:[1,0]
	v_pk_add_f32 v[70:71], v[86:87], 1.0 op_sel_hi:[1,0]
	v_med3_f32 v56, v56, s63, v167
	v_rcp_f32_e32 v70, v70
	v_rcp_f32_e32 v71, v71
	v_med3_f32 v57, v57, s63, v167
	v_pk_add_f32 v[58:59], v[58:59], v[134:135]
	v_pk_fma_f32 v[56:57], v[72:73], v[56:57], v[72:73]
	v_min_f32_e32 v58, 0x40e00000, v58
	v_min_f32_e32 v59, 0x40e00000, v59
	v_pk_mul_f32 v[56:57], v[56:57], v[70:71]
	v_pk_mul_f32 v[70:71], v[58:59], s[26:27] op_sel_hi:[1,0]
	v_pk_add_f32 v[60:61], v[60:61], v[136:137]
	v_exp_f32_e32 v70, v70
	v_exp_f32_e32 v71, v71
	v_min_f32_e32 v60, 0x40e00000, v60
	v_min_f32_e32 v61, 0x40e00000, v61
	v_exp_f32_e32 v76, v76
	v_exp_f32_e32 v77, v77
	v_pk_add_f32 v[70:71], v[70:71], 1.0 op_sel_hi:[1,0]
	v_pk_mul_f32 v[72:73], v[60:61], s[26:27] op_sel_hi:[1,0]
	v_rcp_f32_e32 v70, v70
	v_rcp_f32_e32 v71, v71
	v_exp_f32_e32 v72, v72
	v_exp_f32_e32 v73, v73
	v_pk_add_f32 v[42:43], v[42:43], v[130:131]
	v_pk_add_f32 v[76:77], v[76:77], 1.0 op_sel_hi:[1,0]
	v_med3_f32 v42, v42, s63, v167
	v_med3_f32 v43, v43, s63, v167
	v_pk_fma_f32 v[42:43], v[58:59], v[42:43], v[58:59]
	v_rcp_f32_e32 v76, v76
	v_rcp_f32_e32 v77, v77
	v_pk_mul_f32 v[58:59], v[42:43], v[70:71]
	v_pk_add_f32 v[42:43], v[72:73], 1.0 op_sel_hi:[1,0]
	v_pk_add_f32 v[44:45], v[44:45], v[132:133]
	v_rcp_f32_e32 v42, v42
	v_rcp_f32_e32 v43, v43
	v_med3_f32 v44, v44, s63, v167
	v_med3_f32 v45, v45, s63, v167
	v_pk_add_f32 v[40:41], v[40:41], v[144:145]
	v_pk_mul_f32 v[54:55], v[54:55], v[76:77]
	v_pk_fma_f32 v[44:45], v[60:61], v[44:45], v[60:61]
	v_min_f32_e32 v40, 0x40e00000, v40
	v_min_f32_e32 v41, 0x40e00000, v41
	v_or_b32_e32 v74, 32, v154
	v_pk_mul_f32 v[60:61], v[44:45], v[42:43]
	v_cvt_pk_bf16_f32 v42, v54, v55
	v_pk_mul_f32 v[54:55], v[40:41], s[26:27] op_sel_hi:[1,0]
	v_ashrrev_i32_e32 v75, 31, v74
	v_exp_f32_e32 v54, v54
	v_exp_f32_e32 v55, v55
	v_lshlrev_b64 v[74:75], 12, v[74:75]
	v_lshl_add_u64 v[74:75], s[12:13], 0, v[74:75]
	v_pk_add_f32 v[38:39], v[38:39], v[142:143]
	v_pk_add_f32 v[22:23], v[22:23], v[138:139]
	v_lshl_add_u64 v[70:71], v[74:75], 0, v[112:113]
	v_cvt_pk_bf16_f32 v43, v56, v57
	v_cvt_pk_bf16_f32 v44, v58, v59
	v_cvt_pk_bf16_f32 v45, v60, v61
	v_min_f32_e32 v38, 0x40e00000, v38
	v_min_f32_e32 v39, 0x40e00000, v39
	v_med3_f32 v22, v22, s63, v167
	v_med3_f32 v23, v23, s63, v167
	global_store_dwordx4 v[70:71], v[42:45], off
	v_pk_fma_f32 v[22:23], v[38:39], v[22:23], v[38:39]
	v_pk_add_f32 v[24:25], v[24:25], v[140:141]
	v_pk_mul_f32 v[44:45], v[38:39], s[26:27] op_sel_hi:[1,0]
	v_pk_add_f32 v[38:39], v[54:55], 1.0 op_sel_hi:[1,0]
	v_med3_f32 v24, v24, s63, v167
	v_rcp_f32_e32 v38, v38
	v_rcp_f32_e32 v39, v39
	v_med3_f32 v25, v25, s63, v167
	v_pk_add_f32 v[26:27], v[26:27], v[134:135]
	v_pk_fma_f32 v[24:25], v[40:41], v[24:25], v[40:41]
	v_min_f32_e32 v26, 0x40e00000, v26
	v_min_f32_e32 v27, 0x40e00000, v27
	v_pk_mul_f32 v[24:25], v[24:25], v[38:39]
	v_pk_mul_f32 v[38:39], v[26:27], s[26:27] op_sel_hi:[1,0]
	v_pk_add_f32 v[28:29], v[28:29], v[136:137]
	v_exp_f32_e32 v38, v38
	v_exp_f32_e32 v39, v39
	v_min_f32_e32 v28, 0x40e00000, v28
	v_min_f32_e32 v29, 0x40e00000, v29
	v_pk_mul_f32 v[40:41], v[28:29], s[26:27] op_sel_hi:[1,0]
	v_pk_add_f32 v[38:39], v[38:39], 1.0 op_sel_hi:[1,0]
	v_exp_f32_e32 v44, v44
	v_exp_f32_e32 v45, v45
	v_rcp_f32_e32 v38, v38
	v_rcp_f32_e32 v39, v39
	v_exp_f32_e32 v40, v40
	v_exp_f32_e32 v41, v41
	v_pk_add_f32 v[10:11], v[10:11], v[130:131]
	v_pk_add_f32 v[44:45], v[44:45], 1.0 op_sel_hi:[1,0]
	v_med3_f32 v10, v10, s63, v167
	v_med3_f32 v11, v11, s63, v167
	v_pk_fma_f32 v[10:11], v[26:27], v[10:11], v[26:27]
	v_rcp_f32_e32 v44, v44
	v_pk_mul_f32 v[26:27], v[10:11], v[38:39]
	v_pk_add_f32 v[10:11], v[40:41], 1.0 op_sel_hi:[1,0]
	v_rcp_f32_e32 v45, v45
	v_rcp_f32_e32 v10, v10
	v_rcp_f32_e32 v11, v11
	v_or_b32_e32 v42, 48, v154
	v_pk_add_f32 v[12:13], v[12:13], v[132:133]
	v_ashrrev_i32_e32 v43, 31, v42
	v_med3_f32 v12, v12, s63, v167
	v_med3_f32 v13, v13, s63, v167
	v_lshlrev_b64 v[42:43], 12, v[42:43]
	v_pk_fma_f32 v[12:13], v[28:29], v[12:13], v[28:29]
	v_lshl_add_u64 v[42:43], s[12:13], 0, v[42:43]
	v_pk_mul_f32 v[22:23], v[22:23], v[44:45]
	v_pk_mul_f32 v[28:29], v[12:13], v[10:11]
	v_lshl_add_u64 v[38:39], v[42:43], 0, v[112:113]
	v_cvt_pk_bf16_f32 v10, v22, v23
	v_cvt_pk_bf16_f32 v11, v24, v25
	v_cvt_pk_bf16_f32 v12, v26, v27
	v_cvt_pk_bf16_f32 v13, v28, v29
	global_store_dwordx4 v[38:39], v[10:13], off
	v_pk_add_f32 v[26:27], v[106:107], v[138:139]
	v_pk_add_f32 v[24:25], v[108:109], v[140:141]
	v_pk_add_f32 v[12:13], v[114:115], v[142:143]
	v_pk_add_f32 v[10:11], v[116:117], v[144:145]
	v_min_f32_e32 v12, 0x40e00000, v12
	v_min_f32_e32 v13, 0x40e00000, v13
	v_pk_mul_f32 v[22:23], v[12:13], s[26:27] op_sel_hi:[1,0]
	v_min_f32_e32 v10, 0x40e00000, v10
	v_exp_f32_e32 v22, v22
	v_exp_f32_e32 v23, v23
	v_min_f32_e32 v11, 0x40e00000, v11
	v_pk_mul_f32 v[28:29], v[10:11], s[26:27] op_sel_hi:[1,0]
	v_med3_f32 v26, v26, s63, v167
; __device__ __forceinline__ unsigned cvt_pk_bf16(float lo, float hi) { return cvt2bf(lo, hi); }
;     __device__ __forceinline__ void operator()(const f32x4 (&acc)[2][2][4][2], const Unit& u, int wr, int wc, int fr, int fq, float b1, LAS float* bx) const {
;     ...
; #pragma unroll
;         for (int ai = 0; ai < 2; ++ai)
; #pragma unroll
;             for (int m = 0; m < 4; ++m) {
;                 bf16* rowp = act + (size_t)(row0 + ai * HALF + m * 16) * DM + col0;
;                 float o[8];
; #pragma unroll
;                 for (int n = 0; n < 2; ++n)
; #pragma unroll
;                     for (int j = 0; j < 4; j += 2) {
;                         const f32x4 gb = n ? g1 : g0, ub = n ? u1 : u0;
;                         const f32x2_t hg = f32x2_t{acc[ai][0][m][n][j], acc[ai][0][m][n][j + 1]} + f32x2_t{gb[j], gb[j + 1]};
;                         const f32x2_t hu = f32x2_t{acc[ai][1][m][n][j], acc[ai][1][m][n][j + 1]} + f32x2_t{ub[j], ub[j + 1]};
;                         const f32x2_t gt = {fminf(hg[0], 7.0f), fminf(hg[1], 7.0f)}, up = {fminf(fmaxf(hu[0], -7.0f), 7.0f), fminf(fmaxf(hu[1], -7.0f), 7.0f)};
;                         const f32x2_t t = gt * (-1.702f * 1.4426950408889634f);
;                         const f32x2_t dn = f32x2_t{__builtin_amdgcn_exp2f(t[0]), __builtin_amdgcn_exp2f(t[1])} + 1.0f;
;                         const f32x2_t sg = {__builtin_amdgcn_rcpf(dn[0]), __builtin_amdgcn_rcpf(dn[1])};
;                         const f32x2_t r2 = (up * gt + gt) * sg;
;                         o[n * 4 + j] = r2[0]; o[n * 4 + j + 1] = r2[1]; }
;                 v4u w; w.x = cvt_pk_bf16(o[0], o[1]); w.y = cvt_pk_bf16(o[2], o[3]); w.z = cvt_pk_bf16(o[4], o[5]); w.w = cvt_pk_bf16(o[6], o[7]);
;                 *(v4u*)rowp = w; }
	v_pk_add_f32 v[22:23], v[22:23], 1.0 op_sel_hi:[1,0]
	v_exp_f32_e32 v28, v28
	v_rcp_f32_e32 v22, v22
	v_rcp_f32_e32 v23, v23
	v_exp_f32_e32 v29, v29
	v_med3_f32 v27, v27, s63, v167
	v_pk_fma_f32 v[12:13], v[12:13], v[26:27], v[12:13]
	v_med3_f32 v24, v24, s63, v167
	v_med3_f32 v25, v25, s63, v167
	v_pk_mul_f32 v[12:13], v[12:13], v[22:23]
	v_pk_add_f32 v[22:23], v[28:29], 1.0 op_sel_hi:[1,0]
	v_pk_fma_f32 v[10:11], v[10:11], v[24:25], v[10:11]
	v_pk_add_f32 v[24:25], v[98:99], v[134:135]
	v_rcp_f32_e32 v22, v22
	v_rcp_f32_e32 v23, v23
	v_min_f32_e32 v24, 0x40e00000, v24
	v_min_f32_e32 v25, 0x40e00000, v25
	v_pk_mul_f32 v[26:27], v[24:25], s[26:27] op_sel_hi:[1,0]
	v_pk_mul_f32 v[22:23], v[10:11], v[22:23]
	v_exp_f32_e32 v26, v26
	v_exp_f32_e32 v27, v27
	v_pk_add_f32 v[10:11], v[100:101], v[136:137]
	v_pk_add_f32 v[38:39], v[94:95], v[130:131]
	v_min_f32_e32 v10, 0x40e00000, v10
	v_min_f32_e32 v11, 0x40e00000, v11
	v_pk_add_f32 v[26:27], v[26:27], 1.0 op_sel_hi:[1,0]
	v_pk_mul_f32 v[40:41], v[10:11], s[26:27] op_sel_hi:[1,0]
	v_rcp_f32_e32 v26, v26
	v_rcp_f32_e32 v27, v27
	v_exp_f32_e32 v40, v40
	v_exp_f32_e32 v41, v41
	v_med3_f32 v38, v38, s63, v167
	v_med3_f32 v39, v39, s63, v167
	v_pk_fma_f32 v[24:25], v[24:25], v[38:39], v[24:25]
	v_pk_add_f32 v[28:29], v[96:97], v[132:133]
	v_pk_mul_f32 v[24:25], v[24:25], v[26:27]
	v_pk_add_f32 v[26:27], v[40:41], 1.0 op_sel_hi:[1,0]
	v_med3_f32 v28, v28, s63, v167
	v_rcp_f32_e32 v26, v26
	v_rcp_f32_e32 v27, v27
	v_med3_f32 v29, v29, s63, v167
	v_pk_fma_f32 v[10:11], v[10:11], v[28:29], v[10:11]
	s_mov_b32 s5, 0x80000
	v_pk_mul_f32 v[26:27], v[10:11], v[26:27]
	v_cvt_pk_bf16_f32 v11, v22, v23
	v_add_co_u32_e32 v22, vcc, s5, v110
	v_cvt_pk_bf16_f32 v10, v12, v13
	v_cvt_pk_bf16_f32 v12, v24, v25
	v_cvt_pk_bf16_f32 v13, v26, v27
	v_addc_co_u32_e32 v23, vcc, 0, v111, vcc
	global_store_dwordx4 v[22:23], v[10:13], off
	v_pk_add_f32 v[26:27], v[78:79], v[138:139]
	v_pk_add_f32 v[24:25], v[80:81], v[140:141]
	v_pk_add_f32 v[12:13], v[82:83], v[142:143]
	v_pk_add_f32 v[10:11], v[84:85], v[144:145]
	v_min_f32_e32 v12, 0x40e00000, v12
	v_min_f32_e32 v13, 0x40e00000, v13
	v_pk_mul_f32 v[22:23], v[12:13], s[26:27] op_sel_hi:[1,0]
	v_min_f32_e32 v10, 0x40e00000, v10
	v_exp_f32_e32 v22, v22
	v_exp_f32_e32 v23, v23
	v_min_f32_e32 v11, 0x40e00000, v11
	v_pk_mul_f32 v[28:29], v[10:11], s[26:27] op_sel_hi:[1,0]
	v_med3_f32 v26, v26, s63, v167
	v_pk_add_f32 v[22:23], v[22:23], 1.0 op_sel_hi:[1,0]
	v_exp_f32_e32 v28, v28
	v_rcp_f32_e32 v22, v22
	v_rcp_f32_e32 v23, v23
	v_exp_f32_e32 v29, v29
	v_med3_f32 v27, v27, s63, v167
	v_pk_fma_f32 v[12:13], v[12:13], v[26:27], v[12:13]
	v_med3_f32 v24, v24, s63, v167
	v_med3_f32 v25, v25, s63, v167
	v_pk_mul_f32 v[12:13], v[12:13], v[22:23]
	v_pk_add_f32 v[22:23], v[28:29], 1.0 op_sel_hi:[1,0]
	v_pk_fma_f32 v[10:11], v[10:11], v[24:25], v[10:11]
	v_pk_add_f32 v[24:25], v[66:67], v[134:135]
	v_rcp_f32_e32 v22, v22
	v_rcp_f32_e32 v23, v23
	v_min_f32_e32 v24, 0x40e00000, v24
	v_min_f32_e32 v25, 0x40e00000, v25
	v_pk_mul_f32 v[26:27], v[24:25], s[26:27] op_sel_hi:[1,0]
	v_pk_mul_f32 v[22:23], v[10:11], v[22:23]
	v_exp_f32_e32 v26, v26
	v_exp_f32_e32 v27, v27
	v_pk_add_f32 v[10:11], v[68:69], v[136:137]
	v_pk_add_f32 v[38:39], v[62:63], v[130:131]
	v_min_f32_e32 v10, 0x40e00000, v10
	v_min_f32_e32 v11, 0x40e00000, v11
	v_pk_add_f32 v[26:27], v[26:27], 1.0 op_sel_hi:[1,0]
	v_pk_mul_f32 v[40:41], v[10:11], s[26:27] op_sel_hi:[1,0]
	v_rcp_f32_e32 v26, v26
	v_rcp_f32_e32 v27, v27
	v_exp_f32_e32 v40, v40
	v_exp_f32_e32 v41, v41
	v_med3_f32 v38, v38, s63, v167
	v_med3_f32 v39, v39, s63, v167
	v_pk_fma_f32 v[24:25], v[24:25], v[38:39], v[24:25]
	v_pk_add_f32 v[28:29], v[64:65], v[132:133]
	v_pk_mul_f32 v[24:25], v[24:25], v[26:27]
	v_pk_add_f32 v[26:27], v[40:41], 1.0 op_sel_hi:[1,0]
	v_med3_f32 v28, v28, s63, v167
	v_rcp_f32_e32 v26, v26
	v_rcp_f32_e32 v27, v27
	v_med3_f32 v29, v29, s63, v167
	v_pk_fma_f32 v[10:11], v[10:11], v[28:29], v[10:11]
	s_mov_b32 s5, 0x90000
	v_pk_mul_f32 v[26:27], v[10:11], v[26:27]
	v_cvt_pk_bf16_f32 v11, v22, v23
	v_add_co_u32_e32 v22, vcc, s5, v110
	v_cvt_pk_bf16_f32 v10, v12, v13
	v_cvt_pk_bf16_f32 v12, v24, v25
	v_cvt_pk_bf16_f32 v13, v26, v27
	v_addc_co_u32_e32 v23, vcc, 0, v111, vcc
	global_store_dwordx4 v[22:23], v[10:13], off
	v_pk_add_f32 v[26:27], v[46:47], v[138:139]
	v_pk_add_f32 v[24:25], v[48:49], v[140:141]
	v_pk_add_f32 v[12:13], v[50:51], v[142:143]
	v_pk_add_f32 v[10:11], v[52:53], v[144:145]
	v_min_f32_e32 v12, 0x40e00000, v12
	v_min_f32_e32 v13, 0x40e00000, v13
	v_pk_mul_f32 v[22:23], v[12:13], s[26:27] op_sel_hi:[1,0]
	v_min_f32_e32 v10, 0x40e00000, v10
	v_exp_f32_e32 v22, v22
	v_exp_f32_e32 v23, v23
	v_min_f32_e32 v11, 0x40e00000, v11
	v_pk_mul_f32 v[28:29], v[10:11], s[26:27] op_sel_hi:[1,0]
	v_med3_f32 v26, v26, s63, v167
	v_pk_add_f32 v[22:23], v[22:23], 1.0 op_sel_hi:[1,0]
	v_exp_f32_e32 v28, v28
	v_rcp_f32_e32 v22, v22
	v_rcp_f32_e32 v23, v23
	v_exp_f32_e32 v29, v29
	v_med3_f32 v27, v27, s63, v167
; __device__ __forceinline__ unsigned cvt_pk_bf16(float lo, float hi) { return cvt2bf(lo, hi); }
; template <class Epi, class Sched>
; __device__ __forceinline__ void gemm_phase(LAS unsigned char* lds, const Sched& S, const Epi& E) {
;     ...
;         if (!has_next) break;
; #pragma unroll
;         for (int a = 0; a < 2; ++a)
; #pragma unroll
;             for (int b = 0; b < 2; ++b)
; #pragma unroll
;                 for (int m = 0; m < 4; ++m)
; #pragma unroll
;                     for (int n = 0; n < 2; ++n) acc[a][b][m][n] = (f32x4){0.f, 0.f, 0.f, 0.f};
;         cur = nxt; cA = nA; cB = nB; ++ui;
;         b1 = E.pre(cur, wc, lane);
;         if constexpr (Sched::GATHER) { PG8_GIDX(vg, cur); }
;     __device__ __forceinline__ void operator()(const f32x4 (&acc)[2][2][4][2], const Unit& u, int wr, int wc, int fr, int fq, float b1, LAS float* bx) const {
;     ...
; #pragma unroll
;         for (int ai = 0; ai < 2; ++ai)
; #pragma unroll
;             for (int m = 0; m < 4; ++m) {
;                 bf16* rowp = act + (size_t)(row0 + ai * HALF + m * 16) * DM + col0;
;                 float o[8];
; #pragma unroll
;                 for (int n = 0; n < 2; ++n)
; #pragma unroll
;                     for (int j = 0; j < 4; j += 2) {
;                         const f32x4 gb = n ? g1 : g0, ub = n ? u1 : u0;
;                         const f32x2_t hg = f32x2_t{acc[ai][0][m][n][j], acc[ai][0][m][n][j + 1]} + f32x2_t{gb[j], gb[j + 1]};
;                         const f32x2_t hu = f32x2_t{acc[ai][1][m][n][j], acc[ai][1][m][n][j + 1]} + f32x2_t{ub[j], ub[j + 1]};
;                         const f32x2_t gt = {fminf(hg[0], 7.0f), fminf(hg[1], 7.0f)}, up = {fminf(fmaxf(hu[0], -7.0f), 7.0f), fminf(fmaxf(hu[1], -7.0f), 7.0f)};
;                         const f32x2_t t = gt * (-1.702f * 1.4426950408889634f);
;                         const f32x2_t dn = f32x2_t{__builtin_amdgcn_exp2f(t[0]), __builtin_amdgcn_exp2f(t[1])} + 1.0f;
;                         const f32x2_t sg = {__builtin_amdgcn_rcpf(dn[0]), __builtin_amdgcn_rcpf(dn[1])};
;                         const f32x2_t r2 = (up * gt + gt) * sg;
;                         o[n * 4 + j] = r2[0]; o[n * 4 + j + 1] = r2[1]; }
;                 v4u w; w.x = cvt_pk_bf16(o[0], o[1]); w.y = cvt_pk_bf16(o[2], o[3]); w.z = cvt_pk_bf16(o[4], o[5]); w.w = cvt_pk_bf16(o[6], o[7]);
;                 *(v4u*)rowp = w; }
	v_pk_fma_f32 v[12:13], v[12:13], v[26:27], v[12:13]
	v_med3_f32 v24, v24, s63, v167
	v_med3_f32 v25, v25, s63, v167
	v_pk_mul_f32 v[12:13], v[12:13], v[22:23]
	v_pk_add_f32 v[22:23], v[28:29], 1.0 op_sel_hi:[1,0]
	v_pk_fma_f32 v[10:11], v[10:11], v[24:25], v[10:11]
	v_pk_add_f32 v[24:25], v[34:35], v[134:135]
	v_rcp_f32_e32 v22, v22
	v_rcp_f32_e32 v23, v23
	v_min_f32_e32 v24, 0x40e00000, v24
	v_min_f32_e32 v25, 0x40e00000, v25
	v_pk_mul_f32 v[26:27], v[24:25], s[26:27] op_sel_hi:[1,0]
	v_pk_mul_f32 v[22:23], v[10:11], v[22:23]
	v_exp_f32_e32 v26, v26
	v_exp_f32_e32 v27, v27
	v_pk_add_f32 v[10:11], v[36:37], v[136:137]
	v_pk_add_f32 v[28:29], v[32:33], v[132:133]
	v_min_f32_e32 v10, 0x40e00000, v10
	v_min_f32_e32 v11, 0x40e00000, v11
	v_pk_add_f32 v[26:27], v[26:27], 1.0 op_sel_hi:[1,0]
	v_pk_mul_f32 v[32:33], v[10:11], s[26:27] op_sel_hi:[1,0]
	v_rcp_f32_e32 v26, v26
	v_rcp_f32_e32 v27, v27
	v_exp_f32_e32 v32, v32
	v_exp_f32_e32 v33, v33
	v_pk_add_f32 v[30:31], v[30:31], v[130:131]
	v_med3_f32 v28, v28, s63, v167
	v_med3_f32 v30, v30, s63, v167
	v_med3_f32 v31, v31, s63, v167
	v_pk_fma_f32 v[24:25], v[24:25], v[30:31], v[24:25]
	v_med3_f32 v29, v29, s63, v167
	v_pk_mul_f32 v[24:25], v[24:25], v[26:27]
	v_pk_add_f32 v[26:27], v[32:33], 1.0 op_sel_hi:[1,0]
	v_pk_fma_f32 v[10:11], v[10:11], v[28:29], v[10:11]
	v_rcp_f32_e32 v26, v26
	v_rcp_f32_e32 v27, v27
	s_mov_b32 s5, 0xa0000
	v_pk_add_f32 v[14:15], v[14:15], v[138:139]
	v_pk_add_f32 v[16:17], v[16:17], v[140:141]
	v_pk_mul_f32 v[26:27], v[10:11], v[26:27]
	v_cvt_pk_bf16_f32 v11, v22, v23
	v_add_co_u32_e32 v22, vcc, s5, v110
	v_cvt_pk_bf16_f32 v10, v12, v13
	v_cvt_pk_bf16_f32 v12, v24, v25
	v_cvt_pk_bf16_f32 v13, v26, v27
	v_addc_co_u32_e32 v23, vcc, 0, v111, vcc
	global_store_dwordx4 v[22:23], v[10:13], off
	v_med3_f32 v14, v14, s63, v167
	v_med3_f32 v15, v15, s63, v167
	v_pk_add_f32 v[10:11], v[20:21], v[144:145]
	v_pk_add_f32 v[12:13], v[18:19], v[142:143]
	v_min_f32_e32 v10, 0x40e00000, v10
	v_min_f32_e32 v11, 0x40e00000, v11
	v_pk_mul_f32 v[20:21], v[10:11], s[26:27] op_sel_hi:[1,0]
	v_min_f32_e32 v12, 0x40e00000, v12
	v_exp_f32_e32 v20, v20
	v_exp_f32_e32 v21, v21
	v_min_f32_e32 v13, 0x40e00000, v13
	v_pk_mul_f32 v[18:19], v[12:13], s[26:27] op_sel_hi:[1,0]
	v_pk_fma_f32 v[12:13], v[12:13], v[14:15], v[12:13]
	v_pk_add_f32 v[14:15], v[20:21], 1.0 op_sel_hi:[1,0]
	v_med3_f32 v16, v16, s63, v167
	v_rcp_f32_e32 v14, v14
	v_rcp_f32_e32 v15, v15
	v_med3_f32 v17, v17, s63, v167
	v_pk_add_f32 v[6:7], v[6:7], v[134:135]
	v_pk_fma_f32 v[10:11], v[10:11], v[16:17], v[10:11]
	v_min_f32_e32 v6, 0x40e00000, v6
	v_min_f32_e32 v7, 0x40e00000, v7
	v_pk_mul_f32 v[10:11], v[10:11], v[14:15]
	v_pk_mul_f32 v[14:15], v[6:7], s[26:27] op_sel_hi:[1,0]
	v_pk_add_f32 v[8:9], v[8:9], v[136:137]
	v_exp_f32_e32 v14, v14
	v_exp_f32_e32 v15, v15
	v_min_f32_e32 v8, 0x40e00000, v8
	v_min_f32_e32 v9, 0x40e00000, v9
	v_pk_mul_f32 v[16:17], v[8:9], s[26:27] op_sel_hi:[1,0]
	v_pk_add_f32 v[14:15], v[14:15], 1.0 op_sel_hi:[1,0]
	v_exp_f32_e32 v16, v16
	v_rcp_f32_e32 v14, v14
	v_rcp_f32_e32 v15, v15
	v_exp_f32_e32 v17, v17
	v_exp_f32_e32 v18, v18
	v_exp_f32_e32 v19, v19
	v_pk_add_f32 v[2:3], v[2:3], v[130:131]
	v_pk_add_f32 v[4:5], v[4:5], v[132:133]
	v_med3_f32 v2, v2, s63, v167
	v_med3_f32 v3, v3, s63, v167
	v_pk_fma_f32 v[2:3], v[6:7], v[2:3], v[6:7]
	v_pk_add_f32 v[18:19], v[18:19], 1.0 op_sel_hi:[1,0]
	v_pk_mul_f32 v[6:7], v[2:3], v[14:15]
	v_pk_add_f32 v[2:3], v[16:17], 1.0 op_sel_hi:[1,0]
	v_rcp_f32_e32 v18, v18
	v_rcp_f32_e32 v2, v2
	v_rcp_f32_e32 v3, v3
	v_rcp_f32_e32 v19, v19
	v_med3_f32 v4, v4, s63, v167
	v_med3_f32 v5, v5, s63, v167
	v_pk_fma_f32 v[4:5], v[8:9], v[4:5], v[8:9]
	v_pk_mul_f32 v[12:13], v[12:13], v[18:19]
	v_pk_mul_f32 v[8:9], v[4:5], v[2:3]
	v_cvt_pk_bf16_f32 v4, v6, v7
	v_add_co_u32_e32 v6, vcc, 0xb0000, v110
	v_cvt_pk_bf16_f32 v2, v12, v13
	s_nop 0
	v_addc_co_u32_e32 v7, vcc, 0, v111, vcc
	v_cvt_pk_bf16_f32 v3, v10, v11
	v_cvt_pk_bf16_f32 v5, v8, v9
	s_andn2_b64 vcc, exec, s[34:35]
	s_mov_b64 s[18:19], -1
	global_store_dwordx4 v[6:7], v[2:5], off
	s_cbranch_vccnz .LBB0_1250
	s_ashr_i32 s29, s28, 31
	s_lshl_b32 s14, s4, 7
	s_ashr_i32 s15, s14, 31
	s_lshl_b64 s[18:19], s[28:29], 14
	s_add_u32 s5, s50, s18
	s_addc_u32 s18, s51, s19
	s_lshl_b64 s[14:15], s[14:15], 2
	s_add_u32 s5, s5, s14
	s_addc_u32 s15, s18, s15
	s_add_u32 s14, s5, s37
	s_addc_u32 s15, s15, 0
	v_lshl_add_u64 v[2:3], s[14:15], 0, v[148:149]
	v_mov_b32_e32 v153, v149
	v_lshl_add_u64 v[2:3], v[2:3], 0, v[152:153]
	global_load_dword v130, v[2:3], off
	s_sub_i32 s5, s82, s54
	v_med3_i32 v2, s5, 0, 47
	v_lshl_add_u32 v2, v2, 9, v163
	v_lshl_add_u32 v3, v164, 1, v2
	v_lshl_add_u32 v2, v165, 1, v2
	ds_read_u16 v4, v3
	ds_read_u16 v3, v3 offset:256
	ds_read_u16 v5, v2
	ds_read_u16 v2, v2 offset:256
	s_mov_b64 s[18:19], 0
	s_waitcnt lgkmcnt(3)
	v_lshl_or_b32 v131, v4, 12, v147
	s_waitcnt lgkmcnt(2)
	v_lshl_or_b32 v132, v3, 12, v147
	s_waitcnt lgkmcnt(1)
	v_lshl_or_b32 v133, v5, 12, v147
	s_waitcnt lgkmcnt(0)
	v_lshl_or_b32 v134, v2, 12, v147

; #define LAS __attribute__((address_space(3)))
; __device__ __forceinline__ unsigned cvt_pk_bf16(float lo, float hi) { return cvt2bf(lo, hi); }
;     __device__ __forceinline__ void operator()(const f32x4 (&acc)[2][2][4][2], const Unit& u, int wr, int wc, int fr, int fq, float b1, LAS float* bx) const {
;         const int row0 = u.pm * BM + wr * 64 + fr, col0 = u.pn * BM + wc * 32 + 8 * fq;
;         bx[threadIdx.x & 63] = b1;
;         f32x4 bv[2][2];
; #pragma unroll
;         for (int bj = 0; bj < 2; ++bj)
; #pragma unroll
;             for (int n = 0; n < 2; ++n) bv[bj][n] = *(const LAS f32x4*)(bx + bj * 32 + 8 * fq + 4 * n);
; #pragma unroll
;         for (int ai = 0; ai < 2; ++ai)
; #pragma unroll
;             for (int m = 0; m < 4; ++m) { bf16* rowp = ys + (size_t)(row0 + ai * HALF + m * 16) * DM + col0;
; #pragma unroll
;                 for (int bj = 0; bj < 2; ++bj) { const f32x4 v0 = acc[ai][bj][m][0] + bv[bj][0], v1 = acc[ai][bj][m][1] + bv[bj][1];
;                     v4u w; w.x = cvt_pk_bf16(v0[0], v0[1]); w.y = cvt_pk_bf16(v0[2], v0[3]); w.z = cvt_pk_bf16(v1[0], v1[1]); w.w = cvt_pk_bf16(v1[2], v1[3]);
;                     *(v4u*)(rowp + bj * HALF) = w; } }
.LBB0_1463:
	v_lshl_add_u32 v164, s42, 8, v155
	s_waitcnt vmcnt(8)
	ds_write_b32 v156, v130
	ds_read_b128 v[142:145], v157
	ds_read_b128 v[138:141], v157 offset:16
	ds_read_b128 v[134:137], v157 offset:128
	ds_read_b128 v[130:133], v157 offset:144
	v_lshl_or_b32 v150, s40, 8, v158
	v_ashrrev_i32_e32 v165, 31, v164
	v_ashrrev_i32_e32 v151, 31, v150
	v_lshlrev_b64 v[166:167], 12, v[164:165]
	v_lshl_add_u64 v[166:167], s[14:15], 0, v[166:167]
	v_lshlrev_b64 v[168:169], 1, v[150:151]
	v_lshl_add_u64 v[150:151], v[166:167], 0, v[168:169]
	s_waitcnt lgkmcnt(3)
	v_pk_add_f32 v[64:65], v[64:65], v[144:145]
	v_pk_add_f32 v[62:63], v[62:63], v[142:143]
	s_waitcnt lgkmcnt(2)
	v_pk_add_f32 v[166:167], v[60:61], v[140:141]
	v_pk_add_f32 v[60:61], v[58:59], v[138:139]
	v_cvt_pk_bf16_f32 v58, v62, v63
	v_cvt_pk_bf16_f32 v59, v64, v65
	v_cvt_pk_bf16_f32 v60, v60, v61
	v_cvt_pk_bf16_f32 v61, v166, v167
	global_store_dwordx4 v[150:151], v[58:61], off
	s_waitcnt lgkmcnt(1)
	v_pk_add_f32 v[48:49], v[48:49], v[136:137]
	v_pk_add_f32 v[46:47], v[46:47], v[134:135]
	s_waitcnt lgkmcnt(0)
	v_pk_add_f32 v[58:59], v[44:45], v[132:133]
	v_pk_add_f32 v[44:45], v[42:43], v[130:131]
	v_cvt_pk_bf16_f32 v42, v46, v47
	v_cvt_pk_bf16_f32 v43, v48, v49
	v_cvt_pk_bf16_f32 v44, v44, v45
	v_cvt_pk_bf16_f32 v45, v58, v59
	global_store_dwordx4 v[150:151], v[42:45], off offset:256
	v_pk_add_f32 v[48:49], v[52:53], v[140:141]
	v_pk_add_f32 v[50:51], v[50:51], v[138:139]
	v_or_b32_e32 v42, 16, v164
	v_ashrrev_i32_e32 v43, 31, v42
	v_lshlrev_b64 v[42:43], 12, v[42:43]
	v_lshl_add_u64 v[42:43], s[14:15], 0, v[42:43]
	v_lshl_add_u64 v[46:47], v[42:43], 0, v[168:169]
	v_pk_add_f32 v[44:45], v[56:57], v[144:145]
	v_pk_add_f32 v[42:43], v[54:55], v[142:143]
	v_pk_add_f32 v[32:33], v[32:33], v[136:137]
	v_cvt_pk_bf16_f32 v42, v42, v43
	v_cvt_pk_bf16_f32 v43, v44, v45
	v_cvt_pk_bf16_f32 v44, v50, v51
	v_cvt_pk_bf16_f32 v45, v48, v49
	global_store_dwordx4 v[46:47], v[42:45], off
	v_pk_add_f32 v[30:31], v[30:31], v[134:135]
	v_pk_add_f32 v[34:35], v[34:35], v[138:139]
	v_pk_add_f32 v[42:43], v[28:29], v[132:133]
	v_pk_add_f32 v[28:29], v[26:27], v[130:131]
	v_cvt_pk_bf16_f32 v26, v30, v31
	v_cvt_pk_bf16_f32 v27, v32, v33
	v_cvt_pk_bf16_f32 v28, v28, v29
	v_cvt_pk_bf16_f32 v29, v42, v43
	global_store_dwordx4 v[46:47], v[26:29], off offset:256
	v_pk_add_f32 v[32:33], v[36:37], v[140:141]
	s_cmp_eq_u64 s[16:17], 0
	s_cbranch_scc1 .Lp6_al
	s_barrier
; #define LAS __attribute__((address_space(3)))
; __device__ __forceinline__ unsigned cvt_pk_bf16(float lo, float hi) { return cvt2bf(lo, hi); }
; #define PG8_BAR __builtin_amdgcn_s_barrier()
; template <class Epi, class Sched>
; __device__ __forceinline__ void gemm_phase(LAS unsigned char* lds, const Sched& S, const Epi& E) {
;     ...
;         if (!has_next) break;
; #pragma unroll
;         for (int a = 0; a < 2; ++a)
; #pragma unroll
;             for (int b = 0; b < 2; ++b)
; #pragma unroll
;                 for (int m = 0; m < 4; ++m)
; #pragma unroll
;                     for (int n = 0; n < 2; ++n) acc[a][b][m][n] = (f32x4){0.f, 0.f, 0.f, 0.f};
;         cur = nxt; cA = nA; cB = nB; ++ui;
;         b1 = E.pre(cur, wc, lane);
;         if constexpr (Sched::GATHER) { PG8_GIDX(vg, cur); }
;         if constexpr (Epi::ALIGN) { if (wr == 1) PG8_BAR; }
;     __device__ __forceinline__ void operator()(const f32x4 (&acc)[2][2][4][2], const Unit& u, int wr, int wc, int fr, int fq, float b1, LAS float* bx) const {
;         const int row0 = u.pm * BM + wr * 64 + fr, col0 = u.pn * BM + wc * 32 + 8 * fq;
;         bx[threadIdx.x & 63] = b1;
;         f32x4 bv[2][2];
; #pragma unroll
;         for (int bj = 0; bj < 2; ++bj)
; #pragma unroll
;             for (int n = 0; n < 2; ++n) bv[bj][n] = *(const LAS f32x4*)(bx + bj * 32 + 8 * fq + 4 * n);
; #pragma unroll
;         for (int ai = 0; ai < 2; ++ai)
; #pragma unroll
;             for (int m = 0; m < 4; ++m) { bf16* rowp = ys + (size_t)(row0 + ai * HALF + m * 16) * DM + col0;
; #pragma unroll
;                 for (int bj = 0; bj < 2; ++bj) { const f32x4 v0 = acc[ai][bj][m][0] + bv[bj][0], v1 = acc[ai][bj][m][1] + bv[bj][1];
;                     v4u w; w.x = cvt_pk_bf16(v0[0], v0[1]); w.y = cvt_pk_bf16(v0[2], v0[3]); w.z = cvt_pk_bf16(v1[0], v1[1]); w.w = cvt_pk_bf16(v1[2], v1[3]);
;                     *(v4u*)(rowp + bj * HALF) = w; } }
.Lp6_al:
	v_pk_add_f32 v[16:17], v[16:17], v[136:137]
	v_or_b32_e32 v26, 32, v164
	v_ashrrev_i32_e32 v27, 31, v26
	v_lshlrev_b64 v[26:27], 12, v[26:27]
	v_lshl_add_u64 v[26:27], s[14:15], 0, v[26:27]
	v_lshl_add_u64 v[30:31], v[26:27], 0, v[168:169]
	v_pk_add_f32 v[28:29], v[40:41], v[144:145]
	v_pk_add_f32 v[26:27], v[38:39], v[142:143]
	v_pk_add_f32 v[14:15], v[14:15], v[134:135]
	v_cvt_pk_bf16_f32 v26, v26, v27
	v_cvt_pk_bf16_f32 v27, v28, v29
	v_cvt_pk_bf16_f32 v28, v34, v35
	v_cvt_pk_bf16_f32 v29, v32, v33
	global_store_dwordx4 v[30:31], v[26:29], off
	v_pk_add_f32 v[18:19], v[18:19], v[138:139]
	v_pk_add_f32 v[8:9], v[8:9], v[136:137]
	v_pk_add_f32 v[26:27], v[12:13], v[132:133]
	v_pk_add_f32 v[12:13], v[10:11], v[130:131]
	v_cvt_pk_bf16_f32 v10, v14, v15
	v_cvt_pk_bf16_f32 v11, v16, v17
	v_cvt_pk_bf16_f32 v12, v12, v13
	v_cvt_pk_bf16_f32 v13, v26, v27
	global_store_dwordx4 v[30:31], v[10:13], off offset:256
	v_pk_add_f32 v[16:17], v[20:21], v[140:141]
	v_pk_add_f32 v[6:7], v[6:7], v[134:135]
	v_or_b32_e32 v10, 48, v164
	v_ashrrev_i32_e32 v11, 31, v10
	v_lshlrev_b64 v[10:11], 12, v[10:11]
	v_lshl_add_u64 v[10:11], s[14:15], 0, v[10:11]
	v_lshl_add_u64 v[14:15], v[10:11], 0, v[168:169]
	v_pk_add_f32 v[12:13], v[24:25], v[144:145]
	v_pk_add_f32 v[10:11], v[22:23], v[142:143]
	s_mov_b64 s[10:11], -1
	v_cvt_pk_bf16_f32 v10, v10, v11
	v_cvt_pk_bf16_f32 v11, v12, v13
	v_cvt_pk_bf16_f32 v12, v18, v19
	v_cvt_pk_bf16_f32 v13, v16, v17
	global_store_dwordx4 v[14:15], v[10:13], off
	s_nop 1
	v_pk_add_f32 v[10:11], v[4:5], v[132:133]
	v_pk_add_f32 v[4:5], v[2:3], v[130:131]
	v_cvt_pk_bf16_f32 v2, v6, v7
	v_cvt_pk_bf16_f32 v3, v8, v9
	v_cvt_pk_bf16_f32 v4, v4, v5
	v_cvt_pk_bf16_f32 v5, v10, v11
	global_store_dwordx4 v[14:15], v[2:5], off offset:256
	v_pk_add_f32 v[8:9], v[124:125], v[140:141]
	v_pk_add_f32 v[10:11], v[122:123], v[138:139]
	v_pk_add_f32 v[4:5], v[128:129], v[144:145]
	v_pk_add_f32 v[2:3], v[126:127], v[142:143]
	v_lshl_add_u64 v[6:7], v[150:151], 0, s[18:19]
	v_cvt_pk_bf16_f32 v2, v2, v3
	v_cvt_pk_bf16_f32 v3, v4, v5
	v_cvt_pk_bf16_f32 v5, v8, v9
	v_add_co_u32_e32 v8, vcc, s60, v150
	v_cvt_pk_bf16_f32 v4, v10, v11
	s_nop 0
	v_addc_co_u32_e32 v9, vcc, 0, v151, vcc
	global_store_dwordx4 v[8:9], v[2:5], off
	v_pk_add_f32 v[8:9], v[116:117], v[132:133]
	v_pk_add_f32 v[10:11], v[114:115], v[130:131]
	v_pk_add_f32 v[4:5], v[120:121], v[136:137]
	v_pk_add_f32 v[2:3], v[118:119], v[134:135]
	s_nop 0
	v_cvt_pk_bf16_f32 v2, v2, v3
	v_cvt_pk_bf16_f32 v3, v4, v5
	v_cvt_pk_bf16_f32 v4, v10, v11
	v_cvt_pk_bf16_f32 v5, v8, v9
	global_store_dwordx4 v[6:7], v[2:5], off offset:256
	v_pk_add_f32 v[8:9], v[108:109], v[140:141]
	v_pk_add_f32 v[10:11], v[106:107], v[138:139]
	v_pk_add_f32 v[4:5], v[112:113], v[144:145]
	v_pk_add_f32 v[2:3], v[110:111], v[142:143]
	v_lshl_add_u64 v[6:7], v[150:151], 0, s[20:21]
	v_cvt_pk_bf16_f32 v2, v2, v3
	v_cvt_pk_bf16_f32 v3, v4, v5
	v_cvt_pk_bf16_f32 v5, v8, v9
	v_add_co_u32_e32 v8, vcc, s69, v150
	v_cvt_pk_bf16_f32 v4, v10, v11
	s_nop 0
	v_addc_co_u32_e32 v9, vcc, 0, v151, vcc
	global_store_dwordx4 v[8:9], v[2:5], off
	v_pk_add_f32 v[8:9], v[100:101], v[132:133]
	v_pk_add_f32 v[10:11], v[98:99], v[130:131]
	v_pk_add_f32 v[4:5], v[104:105], v[136:137]
	v_pk_add_f32 v[2:3], v[102:103], v[134:135]
	s_nop 0
	v_cvt_pk_bf16_f32 v2, v2, v3
	v_cvt_pk_bf16_f32 v3, v4, v5
	v_cvt_pk_bf16_f32 v4, v10, v11
	v_cvt_pk_bf16_f32 v5, v8, v9
	global_store_dwordx4 v[6:7], v[2:5], off offset:256
	v_pk_add_f32 v[8:9], v[92:93], v[140:141]
	v_pk_add_f32 v[10:11], v[90:91], v[138:139]
	v_pk_add_f32 v[4:5], v[96:97], v[144:145]
	v_pk_add_f32 v[2:3], v[94:95], v[142:143]
	v_lshl_add_u64 v[6:7], v[150:151], 0, s[22:23]
	v_cvt_pk_bf16_f32 v2, v2, v3
	v_cvt_pk_bf16_f32 v3, v4, v5
	v_cvt_pk_bf16_f32 v5, v8, v9
	v_add_co_u32_e32 v8, vcc, s70, v150
	v_cvt_pk_bf16_f32 v4, v10, v11
	s_nop 0
	v_addc_co_u32_e32 v9, vcc, 0, v151, vcc
	global_store_dwordx4 v[8:9], v[2:5], off
	v_pk_add_f32 v[8:9], v[84:85], v[132:133]
	v_pk_add_f32 v[10:11], v[82:83], v[130:131]
	v_pk_add_f32 v[4:5], v[88:89], v[136:137]
	v_pk_add_f32 v[2:3], v[86:87], v[134:135]
	s_nop 0
	v_cvt_pk_bf16_f32 v2, v2, v3
	v_cvt_pk_bf16_f32 v3, v4, v5
	v_cvt_pk_bf16_f32 v4, v10, v11
	v_cvt_pk_bf16_f32 v5, v8, v9
	global_store_dwordx4 v[6:7], v[2:5], off offset:256
	v_pk_add_f32 v[8:9], v[76:77], v[140:141]
	v_pk_add_f32 v[10:11], v[74:75], v[138:139]
	v_pk_add_f32 v[4:5], v[80:81], v[144:145]
	v_pk_add_f32 v[2:3], v[78:79], v[142:143]
	v_lshl_add_u64 v[6:7], v[150:151], 0, s[24:25]
	v_cvt_pk_bf16_f32 v2, v2, v3
	v_cvt_pk_bf16_f32 v3, v4, v5
	v_cvt_pk_bf16_f32 v5, v8, v9
	v_add_co_u32_e32 v8, vcc, s71, v150
	v_cvt_pk_bf16_f32 v4, v10, v11
	s_nop 0
	v_addc_co_u32_e32 v9, vcc, 0, v151, vcc
	global_store_dwordx4 v[8:9], v[2:5], off
	v_pk_add_f32 v[8:9], v[68:69], v[132:133]
	v_pk_add_f32 v[10:11], v[66:67], v[130:131]
	v_pk_add_f32 v[4:5], v[72:73], v[136:137]
	v_pk_add_f32 v[2:3], v[70:71], v[134:135]
	s_andn2_b64 vcc, exec, s[38:39]
	v_cvt_pk_bf16_f32 v2, v2, v3
	v_cvt_pk_bf16_f32 v3, v4, v5
	v_cvt_pk_bf16_f32 v4, v10, v11
	v_cvt_pk_bf16_f32 v5, v8, v9
	global_store_dwordx4 v[6:7], v[2:5], off offset:256
	s_cbranch_vccnz .LBB0_1446
	s_ashr_i32 s31, s30, 31
	s_lshl_b32 s10, s26, 8
	v_readlane_b32 s44, v246, 0
	s_ashr_i32 s11, s10, 31
	s_lshl_b64 s[38:39], s[30:31], 13
	v_readlane_b32 s46, v246, 2
	v_readlane_b32 s47, v246, 3
	s_add_u32 s27, s46, s38
	s_addc_u32 s31, s47, s39
	s_lshl_b64 s[10:11], s[10:11], 2
	s_add_u32 s10, s27, s10
	s_addc_u32 s11, s31, s11
	s_add_u32 s10, s10, s41
	s_addc_u32 s11, s11, 0
	v_lshl_add_u64 v[2:3], s[10:11], 0, v[146:147]
	v_mov_b32_e32 v149, v147
	v_lshl_add_u64 v[2:3], v[2:3], 0, v[148:149]
	global_load_dword v130, v[2:3], off
	s_andn2_b64 vcc, exec, s[12:13]
	v_readlane_b32 s45, v246, 1
	v_readlane_b32 s48, v246, 4
	v_readlane_b32 s49, v246, 5
	v_readlane_b32 s50, v246, 6
	v_readlane_b32 s51, v246, 7
	s_cbranch_vccnz .LBB0_1445
	s_barrier
	s_branch .LBB0_1445
